# best9 + expert conversion re-split: PRO converts no experts, H0-shadow converters take experts 0-2, REC idle WGs take experts 3-7
# speedup vs baseline: 1.0155x; 1.0155x over previous
_Z10hybrid_fwd4Args:
	s_load_dwordx8 s[52:59], s[0:1], 0x100
	s_load_dwordx2 s[76:77], s[0:1], 0x120
	s_mov_b32 s96, s2
	v_cmp_gt_u32_e64 s[4:5], 64, v0
	s_and_saveexec_b64 s[2:3], s[4:5]
	v_lshl_add_u32 v1, v0, 2, 0
	v_add_u32_e32 v1, 0x26000, v1
	v_mov_b32_e32 v2, 0
	ds_write_b32 v1, v2
	s_or_b64 exec, exec, s[2:3]
	s_load_dwordx16 s[8:23], s[0:1], 0x40
	s_load_dwordx16 s[80:95], s[0:1], 0xc0
	s_waitcnt lgkmcnt(0)
	s_mov_b32 s98, 0
	s_mov_b32 s99, 0
	s_mov_b32 s100, 0
	s_barrier
	v_writelane_b32 v239, s8, 0
	s_getreg_b32 s2, hwreg(HW_REG_XCC_ID, 0, 4)
	s_and_b32 s78, s2, 15
	v_writelane_b32 v239, s9, 1
	v_writelane_b32 v239, s10, 2
	v_writelane_b32 v239, s11, 3
	v_writelane_b32 v239, s12, 4
	v_writelane_b32 v239, s13, 5
	v_writelane_b32 v239, s14, 6
	v_writelane_b32 v239, s15, 7
	v_writelane_b32 v239, s16, 8
	v_writelane_b32 v239, s17, 9
	v_writelane_b32 v239, s18, 10
	v_writelane_b32 v239, s19, 11
	v_writelane_b32 v239, s20, 12
	v_writelane_b32 v239, s21, 13
	v_writelane_b32 v239, s22, 14
	v_writelane_b32 v239, s23, 15
	v_cmp_eq_u32_e64 s[6:7], 0, v0
	s_mov_b64 s[2:3], exec
	s_nop 0
	v_writelane_b32 v239, s6, 16
	s_nop 1
	v_writelane_b32 v239, s7, 17
	s_and_b64 s[6:7], s[2:3], s[6:7]
	s_mov_b64 exec, s[6:7]
	s_cbranch_execz .LBB0_5
	s_mov_b64 s[6:7], exec
	v_mbcnt_lo_u32_b32 v1, s6, 0
	v_mbcnt_hi_u32_b32 v1, s7, v1
	v_cmp_eq_u32_e32 vcc, 0, v1
	s_and_b64 s[8:9], exec, vcc
	s_mov_b64 exec, s[8:9]
	s_cbranch_execz .LBB0_5
	s_lshl_b32 s8, s78, 8
	s_bcnt1_i32_b64 s6, s[6:7]
	v_mov_b32_e32 v1, s8
	v_mov_b32_e32 v2, s6
	global_atomic_add v1, v2, s[58:59] offset:1024

.Lconv_entry:
	s_movk_i32 s0, 0x4200
	v_lshl_or_b32 v69, s96, 3, v186
	v_mad_u32_u24 v31, v186, s0, 0
	s_movk_i32 s0, 0xe00
	v_and_b32_e32 v1, 7, v0
	v_cmp_gt_i32_e32 vcc, s0, v69
	v_bfe_u32 v66, v0, 3, 3
	v_mov_b32_e32 v3, 0
	v_lshlrev_b32_e32 v2, 4, v1
	s_movk_i32 s0, 0x840
	s_lshl_b32 s20, s96, 10
	v_lshlrev_b32_e32 v78, 2, v1
	v_add_u32_e32 v79, v31, v2
	v_mul_u32_u24_e32 v4, 0x84, v66
	v_mad_u32_u24 v1, v1, s0, v31
	v_lshl_add_u64 v[80:81], s[58:59], 0, v[2:3]
	s_mov_b64 s[0:1], 0x100000
	v_lshl_or_b32 v74, v186, 7, s20
	s_waitcnt lgkmcnt(0)
	s_lshl_b32 s3, s2, 3
	s_mov_b32 s9, 0
	v_lshl_add_u64 v[18:19], v[80:81], 0, s[0:1]
	v_lshl_add_u32 v75, v66, 2, v1
	s_mov_b64 s[0:1], 0x1c100000
	v_or_b32_e32 v1, v74, v66
	s_movk_i32 s21, 0x1c00
	v_add_u32_e32 v40, v79, v4
	v_or_b32_e32 v68, 8, v66
	v_or_b32_e32 v70, 16, v66
	v_or_b32_e32 v72, 24, v66
	v_lshl_add_u64 v[20:21], v[80:81], 0, s[0:1]
	v_lshl_add_u64 v[22:23], s[90:91], 0, v[2:3]
	v_lshl_add_u64 v[24:25], s[92:93], 0, v[2:3]
	v_lshl_add_u64 v[26:27], s[94:95], 0, v[2:3]
	v_mul_lo_u32 v1, v1, s21
	s_mov_b32 s22, 0xe0000
	s_mul_i32 s23, s3, 0xe0000
	s_movk_i32 s24, 0x60
	s_mov_b32 s25, 0xff200000
	s_mov_b32 s26, 0x38000
	s_mov_b32 s27, 0x70000
	s_mov_b32 s28, 0xa8000
	s_mov_b32 s29, 0x118000
	s_mov_b32 s30, 0x150000
	s_mov_b32 s31, 0x188000
	s_mov_b32 s33, 0x1c0000
	s_mov_b32 s34, 0x1f8000
	s_mov_b32 s35, 0x230000
	s_mov_b32 s60, 0x268000
	s_mov_b32 s61, 0x2a0000
	s_mov_b32 s62, 0x2d8000
	s_mov_b32 s63, 0x310000
	s_mov_b32 s64, 0x348000
	v_add_u32_e32 v41, 0x420, v40
	v_add_u32_e32 v42, 0x428, v40
	v_add_u32_e32 v43, 0x840, v40
	v_add_u32_e32 v44, 0x848, v40
	v_add_u32_e32 v45, 0xc60, v40
	v_add_u32_e32 v46, 0xc68, v40
	v_add_u32_e32 v47, 0x1080, v40
	v_add_u32_e32 v48, 0x1088, v40
	v_add_u32_e32 v49, 0x14a0, v40
	v_add_u32_e32 v50, 0x14a8, v40
	v_add_u32_e32 v51, 0x18c0, v40
	v_add_u32_e32 v52, 0x18c8, v40
	v_add_u32_e32 v53, 0x1ce0, v40
	v_add_u32_e32 v54, 0x1ce8, v40
	v_add_u32_e32 v55, 0x2100, v40
	v_add_u32_e32 v56, 0x2108, v40
	v_add_u32_e32 v57, 0x2520, v40
	s_mov_b32 s65, 0xc3e00000
	s_movk_i32 s66, 0xdff
	v_add_u32_e32 v58, 0x2528, v40
	v_add_u32_e32 v59, 0x2940, v40
	v_add_u32_e32 v60, 0x2948, v40
	v_add_u32_e32 v61, 0x2d60, v40
	v_add_u32_e32 v62, 0x2d68, v40
	v_add_u32_e32 v63, 0x3180, v40
	v_add_u32_e32 v64, 0x3188, v40
	v_mov_b32_e32 v65, 0x43e00000
	v_mov_b32_e32 v67, 0x3800000
	s_mov_b32 s8, s98
	s_cmp_lg_u32 s8, s100
	s_cbranch_scc0 .LBB0_15
	s_branch .LBB0_8

.LBB0_400:
	s_cmp_lt_i32 s76, 2
	s_cselect_b64 s[6:7], -1, 0
	s_add_u32 s82, s58, 0x32100000
	s_addc_u32 s83, s59, 0
	s_and_b64 s[0:1], s[6:7], s[0:1]
	s_andn2_b64 vcc, exec, s[0:1]
	s_cbranch_vccnz .LBB0_417
	s_mov_b32 s101, s2
	s_cmpk_lt_i32 s96, 192
	s_cbranch_scc1 .Lh0_gemm
	s_sub_i32 s96, s96, 192
	s_sub_i32 s2, s101, 192
	s_mov_b32 s98, 0
	s_mov_b32 s100, 3
	s_mov_b32 s99, 1
	v_readlane_b32 s6, v239, 34
	v_readlane_b32 s7, v239, 35
	s_nop 3
	s_sub_u32 s6, s6, 0x128
	s_subb_u32 s7, s7, 0
	s_load_dwordx2 s[82:83], s[6:7], 0xc8
	s_waitcnt lgkmcnt(0)
	s_branch .Lconv_entry

.LBB0_1568:
	s_and_b64 vcc, exec, s[0:1]
	s_cbranch_vccz .LBB0_1579
	s_cmpk_lt_i32 s96, 0x50
	s_cbranch_scc1 .LBB0_1579
	s_lshl_b32 s0, s96, 3
	s_addk_i32 s0, 0xfd80
	v_or_b32_e32 v1, s0, v186
	s_movk_i32 s0, 0x4200
	s_waitcnt vmcnt(0)
	v_and_b32_e32 v3, 7, v0
	v_mad_u32_u24 v6, v186, s0, 0
	s_movk_i32 s0, 0xe00
	v_bfe_u32 v18, v0, 3, 3
	v_lshlrev_b32_e32 v2, 4, v3
	v_mul_u32_u24_e32 v9, 0x840, v3
	v_mov_b32_e32 v3, 0
	s_lshl_b32 s3, s2, 3
	v_cmp_gt_i32_e64 s[4:5], s0, v1
	v_add_u32_e32 v7, v6, v2
	v_mul_u32_u24_e32 v8, 0x84, v18
	v_lshl_add_u64 v[4:5], s[58:59], 0, v[2:3]
	s_mov_b64 s[0:1], 0x100000
	s_mov_b32 s21, 0xe0000
	s_addk_i32 s3, 0xfd80
	v_lshl_add_u64 v[26:27], v[4:5], 0, s[0:1]
	v_lshlrev_b32_e32 v10, 2, v18
	s_mov_b64 s[0:1], 0x1c100000
	v_lshl_add_u64 v[30:31], s[90:91], 0, v[2:3]
	v_lshl_add_u64 v[32:33], s[92:93], 0, v[2:3]
	v_lshl_add_u64 v[34:35], s[94:95], 0, v[2:3]
	v_mul_u32_u24_e32 v2, 0x1c00, v18
	v_mul_lo_u32 v3, v1, s21
	v_add_u32_e32 v25, v7, v8
	s_mov_b32 s7, 0
	v_or_b32_e32 v20, 8, v18
	v_or_b32_e32 v22, 16, v18
	v_or_b32_e32 v24, 24, v18
	v_add3_u32 v19, v6, v9, v10
	v_lshl_add_u64 v[28:29], v[4:5], 0, s[0:1]
	s_movk_i32 s20, 0x1c00
	s_mov_b64 s[14:15], 3
	s_mov_b32 s98, 3
	s_mov_b64 s[10:11], 0
	v_or_b32_e32 v21, v2, v3
	s_mul_i32 s22, s3, 0xe0000
	v_lshlrev_b32_e32 v23, 7, v1
	s_lshl_b32 s23, s3, 7
	s_movk_i32 s24, 0x60
	s_mov_b32 s25, 0xff200000
	s_mov_b32 s26, 0x38000
	s_mov_b32 s27, 0x70000
	s_mov_b32 s28, 0xa8000
	s_mov_b32 s29, 0x118000
	s_mov_b32 s30, 0x150000
	s_mov_b32 s31, 0x188000
	s_mov_b32 s33, 0x1c0000
	s_mov_b32 s34, 0x1f8000
	s_mov_b32 s35, 0x230000
	s_mov_b32 s36, 0x268000
	s_mov_b32 s37, 0x2a0000
	s_mov_b32 s38, 0x2d8000
	s_mov_b32 s39, 0x310000
	s_mov_b32 s40, 0x348000
	v_add_u32_e32 v39, 0x420, v25
	v_add_u32_e32 v48, 0x428, v25
	v_add_u32_e32 v49, 0x840, v25
	v_add_u32_e32 v50, 0x848, v25
	v_add_u32_e32 v51, 0xc60, v25
	v_add_u32_e32 v52, 0xc68, v25
	v_add_u32_e32 v53, 0x1080, v25
	v_add_u32_e32 v54, 0x1088, v25
	v_add_u32_e32 v55, 0x14a0, v25
	v_add_u32_e32 v56, 0x14a8, v25
	v_add_u32_e32 v57, 0x18c0, v25
	v_add_u32_e32 v58, 0x18c8, v25
	v_add_u32_e32 v59, 0x1ce0, v25
	v_add_u32_e32 v60, 0x1ce8, v25
	v_add_u32_e32 v61, 0x2100, v25
	v_add_u32_e32 v62, 0x2108, v25
	v_add_u32_e32 v63, 0x2520, v25
	v_add_u32_e32 v64, 0x2528, v25
	v_add_u32_e32 v65, 0x2940, v25
	v_add_u32_e32 v66, 0x2948, v25
	v_add_u32_e32 v67, 0x2d60, v25
	v_add_u32_e32 v68, 0x2d68, v25
	s_mov_b32 s41, 0xc3e00000
	s_movk_i32 s42, 0xdff
	s_mov_b32 s43, 0x92492493
	s_movk_i32 s44, 0xe400
	v_add_u32_e32 v69, 0x3180, v25
	v_add_u32_e32 v70, 0x3188, v25
	v_add_u32_e32 v71, 0x35a0, v25
	v_add_u32_e32 v72, 0x35a8, v25
	v_add_u32_e32 v73, 0x39c0, v25
	v_add_u32_e32 v74, 0x39c8, v25
	v_mov_b32_e32 v75, 0x43e00000
	s_branch .LBB0_1572
